# baseline (speedup 1.0000x reference)
_Z6k_dlrmPKiS0_S0_S0_S0_S0_S0_PKfS2_S2_S2_S2_S2_S2_S2_S2_S2_S2_S2_S2_S2_S2_S2_Pf:
	v_readfirstlane_b32 s33, v0
	s_load_dwordx16 s[40:55], s[0:1], 0x0
	s_load_dwordx16 s[56:71], s[0:1], 0x40
	s_load_dwordx16 s[72:87], s[0:1], 0x80
	s_lshr_b32 s37, s33, 6
	s_lshl_b32 s30, s2, 6
	s_lshl_b32 s34, s37, 2
	v_and_b32_e32 v1, 63, v0
	s_add_i32 s6, s34, s30
	v_lshl_or_b32 v2, s6, 6, v1
	v_ashrrev_i32_e32 v3, 31, v2
	v_and_b32_e32 v17, 31, v0
	v_and_b32_e32 v82, 15, v0
	s_waitcnt lgkmcnt(0)
	s_load_dword s88, s[84:85], 0x0
	v_lshl_add_u64 v[2:3], v[2:3], 2, s[50:51]
	global_load_dword v10, v[2:3], off nt
	global_load_dword v11, v[2:3], off offset:256 nt
	global_load_dword v12, v[2:3], off offset:512 nt
	global_load_dword v14, v[2:3], off offset:768 nt
	v_lshl_or_b32 v2, s6, 3, v17
	v_ashrrev_i32_e32 v3, 31, v2
	v_lshl_add_u64 v[2:3], v[2:3], 2, s[46:47]
	global_load_dword v13, v[2:3], off nt
	v_cmp_gt_u32_e32 vcc, 4, v1
	v_mov_b32_e32 v15, 0
	v_mov_b32_e32 v5, 0
	v_mov_b32_e32 v4, 0
	v_mov_b32_e32 v3, 0
	v_mov_b32_e32 v2, 0
	s_and_saveexec_b64 s[2:3], vcc
	v_or_b32_e32 v2, s6, v1
	v_ashrrev_i32_e32 v3, 31, v2
	v_lshlrev_b64 v[6:7], 2, v[2:3]
	v_lshl_add_u64 v[2:3], s[52:53], 0, v[6:7]
	v_lshl_add_u64 v[4:5], s[48:49], 0, v[6:7]
	global_load_dword v2, v[2:3], off nt
	v_lshl_add_u64 v[8:9], s[42:43], 0, v[6:7]
	global_load_dword v3, v[4:5], off nt
	v_lshl_add_u64 v[4:5], s[40:41], 0, v[6:7]
	v_lshl_add_u64 v[6:7], s[44:45], 0, v[6:7]
	global_load_dword v4, v[4:5], off nt
	s_nop 0
	global_load_dword v5, v[8:9], off nt
	global_load_dword v15, v[6:7], off nt
	s_or_b64 exec, exec, s[2:3]
	v_or_b32_e32 v6, s30, v1
	v_ashrrev_i32_e32 v7, 31, v6
	v_lshl_add_u64 v[6:7], v[6:7], 2, s[54:55]
	global_load_dword v16, v[6:7], off nt
	s_cmp_lt_u32 s37, 4
	s_cbranch_scc1 .Lpro_wl_done
	v_lshrrev_b32_e32 v20, 5, v1
	v_lshlrev_b32_e32 v21, 2, v17
	v_lshl_or_b32 v22, v20, 12, v21
	v_lshl_or_b32 v23, v20, 10, v21
	v_lshrrev_b32_e32 v24, 4, v1
	v_lshlrev_b32_e32 v25, 2, v82
	v_lshl_or_b32 v24, v24, 11, v25
	v_lshlrev_b32_e32 v26, 2, v1
	s_sub_i32 s89, s37, 4
	s_mul_i32 s90, s89, 13
	s_lshr_b32 s90, s90, 6
	s_mul_i32 s91, s90, 5
	s_sub_i32 s91, s89, s91
	s_lshl_b32 s38, s91, 4
	s_add_i32 s38, s38, 15
	s_cmp_lt_u32 s91, 4
	s_cselect_b32 s38, s38, 0
	s_mov_b32 s92, 0
	s_cselect_b32 s93, 0, -1
	s_lshl_b32 s38, s38, 9
	s_lshl_b32 s90, s90, 7
	s_add_u32 s38, s38, s90
	s_add_u32 s90, s74, s38
	s_addc_u32 s91, s75, 0
	global_load_dword v84, v22, s[90:91]
	global_load_dword v85, v22, s[90:91] offset:512
	global_load_dword v86, v22, s[90:91] offset:1024
	global_load_dword v87, v22, s[90:91] offset:1536
	global_load_dword v88, v22, s[90:91] offset:2048
	global_load_dword v89, v22, s[90:91] offset:2560
	global_load_dword v90, v22, s[90:91] offset:3072
	global_load_dword v91, v22, s[90:91] offset:3584
	s_cmp_lt_u32 s37, 12
	s_cbranch_scc0 .Lpro_r1_w2
	s_add_i32 s89, s37, 8
	s_mul_i32 s90, s89, 13
	s_lshr_b32 s90, s90, 6
	s_mul_i32 s91, s90, 5
	s_sub_i32 s91, s89, s91
	s_lshl_b32 s38, s91, 4
	s_add_i32 s38, s38, 15
	s_cmp_lt_u32 s91, 4
	s_cselect_b32 s38, s38, 0
	s_mov_b32 s94, 0
	s_cselect_b32 s95, 0, -1
	s_lshl_b32 s38, s38, 9
	s_lshl_b32 s90, s90, 7
	s_add_u32 s38, s38, s90
	s_add_u32 s90, s74, s38
	s_addc_u32 s91, s75, 0
	global_load_dword v92, v22, s[90:91]
	global_load_dword v93, v22, s[90:91] offset:512
	global_load_dword v94, v22, s[90:91] offset:1024
	global_load_dword v95, v22, s[90:91] offset:1536
	global_load_dword v96, v22, s[90:91] offset:2048
	global_load_dword v97, v22, s[90:91] offset:2560
	global_load_dword v98, v22, s[90:91] offset:3072
	global_load_dword v99, v22, s[90:91] offset:3584
	s_branch .Lpro_r1_done
